# RG phases: per-phase gate-weight copy loop unrolled with its four loads in flight (was load -> vmcnt(0) -> ds_write x4)
# baseline (speedup 1.0000x reference)
.LBB0_348:
	v_mov_b32_e32 v16, v6
	v_lshrrev_b32_e32 v20, 5, v16
	v_ashrrev_i32_e32 v17, 3, v16
	v_and_b32_e32 v20, 0x3fffff0, v20
	v_and_b32_e32 v18, 63, v17
	v_or_b32_e32 v20, s23, v20
	v_lshl_or_b32 v20, v20, 6, v18
	v_ashrrev_i32_e32 v21, 31, v20
	v_lshlrev_b64 v[20:21], 7, v[20:21]
	v_lshl_add_u64 v[20:21], v[4:5], 0, v[20:21]
	global_load_dwordx4 v[20:23], v[20:21], off
	v_mad_u64_u32 v[24:25], s[16:17], v17, s33, v[2:3]
	v_add_u32_e32 v28, 0x200, v6
	v_lshrrev_b32_e32 v32, 5, v28
	v_ashrrev_i32_e32 v29, 3, v28
	v_and_b32_e32 v32, 0x3fffff0, v32
	v_and_b32_e32 v30, 63, v29
	v_or_b32_e32 v32, s23, v32
	v_lshl_or_b32 v32, v32, 6, v30
	v_ashrrev_i32_e32 v33, 31, v32
	v_lshlrev_b64 v[32:33], 7, v[32:33]
	v_lshl_add_u64 v[32:33], v[4:5], 0, v[32:33]
	global_load_dwordx4 v[32:35], v[32:33], off
	v_mad_u64_u32 v[36:37], s[16:17], v29, s33, v[2:3]
	v_add_u32_e32 v40, 0x400, v6
	v_lshrrev_b32_e32 v44, 5, v40
	v_ashrrev_i32_e32 v41, 3, v40
	v_and_b32_e32 v44, 0x3fffff0, v44
	v_and_b32_e32 v42, 63, v41
	v_or_b32_e32 v44, s23, v44
	v_lshl_or_b32 v44, v44, 6, v42
	v_ashrrev_i32_e32 v45, 31, v44
	v_lshlrev_b64 v[44:45], 7, v[44:45]
	v_lshl_add_u64 v[44:45], v[4:5], 0, v[44:45]
	global_load_dwordx4 v[44:47], v[44:45], off
	v_mad_u64_u32 v[48:49], s[16:17], v41, s33, v[2:3]
	v_add_u32_e32 v52, 0x600, v6
	v_lshrrev_b32_e32 v56, 5, v52
	v_ashrrev_i32_e32 v53, 3, v52
	v_and_b32_e32 v56, 0x3fffff0, v56
	v_and_b32_e32 v54, 63, v53
	v_or_b32_e32 v56, s23, v56
	v_lshl_or_b32 v56, v56, 6, v54
	v_ashrrev_i32_e32 v57, 31, v56
	v_lshlrev_b64 v[56:57], 7, v[56:57]
	v_lshl_add_u64 v[56:57], v[4:5], 0, v[56:57]
	global_load_dwordx4 v[56:59], v[56:57], off
	v_mad_u64_u32 v[60:61], s[16:17], v53, s33, v[2:3]
	s_waitcnt vmcnt(0)
	ds_write_b128 v24, v[20:23]
	ds_write_b128 v36, v[32:35]
	ds_write_b128 v48, v[44:47]
	ds_write_b128 v60, v[56:59]

.LBB0_578:
	v_mov_b32_e32 v16, v6
	v_lshrrev_b32_e32 v20, 5, v16
	v_ashrrev_i32_e32 v17, 3, v16
	v_and_b32_e32 v20, 0x3fffff0, v20
	v_and_b32_e32 v18, 63, v17
	v_or_b32_e32 v20, s21, v20
	v_lshl_or_b32 v20, v20, 6, v18
	v_ashrrev_i32_e32 v21, 31, v20
	v_lshlrev_b64 v[20:21], 7, v[20:21]
	v_lshl_add_u64 v[20:21], v[4:5], 0, v[20:21]
	global_load_dwordx4 v[20:23], v[20:21], off
	v_mad_u64_u32 v[24:25], s[18:19], v17, s20, v[2:3]
	v_add_u32_e32 v28, 0x200, v6
	v_lshrrev_b32_e32 v32, 5, v28
	v_ashrrev_i32_e32 v29, 3, v28
	v_and_b32_e32 v32, 0x3fffff0, v32
	v_and_b32_e32 v30, 63, v29
	v_or_b32_e32 v32, s21, v32
	v_lshl_or_b32 v32, v32, 6, v30
	v_ashrrev_i32_e32 v33, 31, v32
	v_lshlrev_b64 v[32:33], 7, v[32:33]
	v_lshl_add_u64 v[32:33], v[4:5], 0, v[32:33]
	global_load_dwordx4 v[32:35], v[32:33], off
	v_mad_u64_u32 v[36:37], s[18:19], v29, s20, v[2:3]
	v_add_u32_e32 v40, 0x400, v6
	v_lshrrev_b32_e32 v44, 5, v40
	v_ashrrev_i32_e32 v41, 3, v40
	v_and_b32_e32 v44, 0x3fffff0, v44
	v_and_b32_e32 v42, 63, v41
	v_or_b32_e32 v44, s21, v44
	v_lshl_or_b32 v44, v44, 6, v42
	v_ashrrev_i32_e32 v45, 31, v44
	v_lshlrev_b64 v[44:45], 7, v[44:45]
	v_lshl_add_u64 v[44:45], v[4:5], 0, v[44:45]
	global_load_dwordx4 v[44:47], v[44:45], off
	v_mad_u64_u32 v[48:49], s[18:19], v41, s20, v[2:3]
	v_add_u32_e32 v52, 0x600, v6
	v_lshrrev_b32_e32 v56, 5, v52
	v_ashrrev_i32_e32 v53, 3, v52
	v_and_b32_e32 v56, 0x3fffff0, v56
	v_and_b32_e32 v54, 63, v53
	v_or_b32_e32 v56, s21, v56
	v_lshl_or_b32 v56, v56, 6, v54
	v_ashrrev_i32_e32 v57, 31, v56
	v_lshlrev_b64 v[56:57], 7, v[56:57]
	v_lshl_add_u64 v[56:57], v[4:5], 0, v[56:57]
	global_load_dwordx4 v[56:59], v[56:57], off
	v_mad_u64_u32 v[60:61], s[18:19], v53, s20, v[2:3]
	s_waitcnt vmcnt(0)
	ds_write_b128 v24, v[20:23]
	ds_write_b128 v36, v[32:35]
	ds_write_b128 v48, v[44:47]
	ds_write_b128 v60, v[56:59]
